# indexer phase: waves 4-7 (the second wave of each SIMD) run at s_setprio 1 for the whole phase so the two waves of a SIMD reach the chunk barrier together; priority reset at the next phase
# speedup vs baseline: 1.0013x; 1.0013x over previous
; #define LAS __attribute__((address_space(3)))
;     __device__ __forceinline__ int lane_() const { return lane_id(); }
;     __device__ __forceinline__ int tid_() const { return wave * 64 + lane_id(); }
; __device__ __forceinline__ void indexer_phase(const Frame& F, const bf16_t* QI, const bf16_t* KI, const float* WI, unsigned* MASK, const pg8::SideConv& SD) {
;     const int tid = F.tid_(), lane = F.lane_(), w = F.wave, r = lane & 31, hi = lane >> 5;
;     LAS unsigned char* lds = F.lds;
;     const float NEG = -__builtin_inff();
;     int sq = 0, spar = 0; bool pend0 = false, pend1 = false; size_t pd0 = 0, pd1 = 0;
;     for (int rnd = 0; rnd < 4; ++rnd) {
;         const int p = (rnd & 1) ? (F.G - 1 - F.bid) : F.bid; const int sidx = rnd * F.G + p;
;         if (sidx >= NB * (SEQ / 16)) continue;
;         const int qg = (SEQ / 16 - 1) - (sidx >> 2), b = sidx & 3;
;         const int q0 = qg * 16, nkeys = q0 + 16, nkt = (nkeys + 31) >> 5, nch = (nkeys + KCH - 1) / KCH;
;         const size_t tb = (size_t)b * SEQ;
;         const int tq = q0 + 2 * w + hi;
;         bf16x8 afr[4];
;         { const int qsel = (r >> 2) & 1, head = (r & 3) + 4 * (r >> 3);
;           const bf16_t* qp = QI + (tb + q0 + 2 * w + qsel) * 1024 + head * 64 + 8 * hi;
; #pragma unroll
;           for (int s = 0; s < 4; ++s) afr[s] = *(const bf16x8*)(qp + 16 * s); }
;         f32x4 wv[4];
; #pragma unroll
;         for (int i = 0; i < 4; ++i) wv[i] = *(const f32x4*)(WI + (tb + tq) * 16 + 4 * i);
;         float sc[128];
; #pragma unroll
;         for (int i = 0; i < 128; ++i) sc[i] = NEG;
;         const int skey = 8 * w + (lane >> 3), ssl = lane & 7;
;         const bf16_t* ksrc = KI + (tb + skey) * 64 + ((ssl ^ ((skey >> 1) & 7)) * 8);
.LBB0_1455:
	s_cmp_lt_i32 s26, 3
	s_cselect_b64 s[0:1], -1, 0
	s_cmp_gt_i32 s27, 2
	s_cselect_b64 s[2:3], -1, 0
	s_and_b64 s[0:1], s[0:1], s[2:3]
	s_andn2_b64 vcc, exec, s[0:1]
	s_cbranch_vccnz .LBB0_1780
	s_cmp_lt_u32 s93, 4
	s_cbranch_scc1 .Lp2prio
	s_setprio 1
.Lp2prio:
	v_mbcnt_lo_u32_b32 v0, -1, 0
	v_mbcnt_hi_u32_b32 v0, -1, v0
	s_waitcnt vmcnt(0)
	v_mbcnt_lo_u32_b32 v64, -1, 0
	v_mbcnt_hi_u32_b32 v64, -1, v64
	v_mov_b32_e32 v71, 0
	v_and_b32_e32 v0, 3, v64
	v_lshrrev_b32_e32 v5, 1, v64
	v_ashrrev_i32_e32 v4, 5, v64
	v_and_or_b32 v0, v5, 12, v0
	s_add_u32 s36, s24, 0x9029000
	v_lshlrev_b32_e32 v0, 7, v0
	v_mov_b32_e32 v1, v71
	v_lshlrev_b32_e32 v2, 3, v4
	s_addc_u32 s37, s25, 0
	v_lshl_add_u64 v[0:1], s[24:25], 0, v[0:1]
	v_ashrrev_i32_e32 v3, 31, v2
	s_add_u32 s28, s24, 0x4d269000
	v_lshl_add_u64 v[0:1], v[2:3], 1, v[0:1]
	s_mov_b64 s[0:1], 0x4b069000
	s_addc_u32 s29, s25, 0
	v_lshl_add_u64 v[72:73], v[0:1], 0, s[0:1]
	s_lshl_b32 s2, s93, 3
	v_ashrrev_i32_e32 v0, 3, v64
	v_add_u32_e32 v74, s2, v0
	v_lshrrev_b32_e32 v6, 1, v74
	v_xor_b32_e32 v0, v6, v64
	v_and_b32_e32 v218, 31, v64
	v_lshlrev_b32_e32 v0, 4, v0
	v_lshlrev_b32_e32 v3, 2, v64
	v_and_b32_e32 v0, 0x70, v0
	v_mov_b32_e32 v1, v71
	v_lshlrev_b32_e32 v2, 7, v218
	v_and_b32_e32 v224, 4, v3
	v_bitop3_b32 v3, v5, v4, 7 bitop3:0x6c
	v_lshl_add_u64 v[0:1], s[24:25], 0, v[0:1]
	s_mov_b64 s[0:1], 0x4d069000
	v_lshl_add_u32 v225, v3, 4, v2
	v_add_u32_e32 v3, 2, v4
	v_lshl_add_u64 v[76:77], v[0:1], 0, s[0:1]
	v_and_b32_e32 v0, 15, v64
	v_bitop3_b32 v3, v3, v5, 7 bitop3:0x78
	v_mul_u32_u24_e32 v220, 0x410, v0
	v_ashrrev_i32_e32 v0, 4, v64
	v_lshl_add_u32 v226, v3, 4, v2
	v_add_u32_e32 v3, 4, v4
	v_lshl_add_u32 v0, s93, 2, v0
	v_bitop3_b32 v3, v3, v5, 7 bitop3:0x78
	v_ashrrev_i32_e32 v1, 31, v0
	v_lshl_add_u32 v227, v3, 4, v2
	v_add_u32_e32 v3, 6, v4
	v_lshlrev_b64 v[66:67], 11, v[0:1]
	v_lshlrev_b32_e32 v0, 3, v64
	v_bitop3_b32 v3, v3, v5, 7 bitop3:0x78
	v_and_b32_e32 v68, 0x78, v0
	v_add_u32_e32 v0, s2, v74
	v_lshl_add_u32 v228, v3, 4, v2
	v_lshlrev_b32_e32 v2, 4, v64
	v_ashrrev_i32_e32 v1, 31, v0
	v_and_b32_e32 v2, 0x70, v2
	v_mov_b32_e32 v3, v71
	v_ashrrev_i32_e32 v65, 31, v64
	s_not_b32 s14, s18
	v_lshl_add_u64 v[2:3], s[68:69], 0, v[2:3]
	v_lshlrev_b64 v[0:1], 14, v[0:1]
	v_ashrrev_i32_e32 v75, 31, v74
	s_add_i32 s63, s19, s14
	v_lshl_add_u64 v[80:81], v[2:3], 0, v[0:1]
	v_lshl_add_u64 v[0:1], v[64:65], 2, s[24:25]
	s_mov_b64 s[14:15], 0x4d369000
	v_lshl_add_u64 v[82:83], v[0:1], 0, s[14:15]
	v_lshlrev_b64 v[0:1], 7, v[74:75]
	v_bitop3_b32 v2, v6, 7, v64 bitop3:0x48
	s_lshl_b32 s39, s93, 1
	s_lshl_b32 s0, s93, 10
	v_lshl_or_b32 v0, v2, 4, v0
	v_add_u32_e32 v222, s39, v4
	s_add_i32 s53, s0, 0
	v_ashrrev_i32_e32 v219, 2, v64
	v_mov_b32_e32 v69, v71
	v_lshl_add_u64 v[4:5], s[36:37], 0, v[66:67]
	v_lshl_add_u64 v[84:85], s[24:25], 0, v[0:1]
	v_mbcnt_lo_u32_b32 v0, -1, 0
	v_bfe_u32 v70, v64, 2, 1
	s_mov_b32 s31, 0
	s_lshl_b32 s38, s93, 4
	v_and_b32_e32 v221, -4, v219
	s_mul_i32 s62, s93, 0x820
	v_cmp_gt_u32_e64 s[0:1], 32, v64
	v_cmp_lt_i32_e64 s[2:3], 0, v64
	v_cmp_gt_i32_e64 s[4:5], 2, v64
	v_cmp_gt_i32_e64 s[6:7], 4, v64
	v_cmp_gt_i32_e64 s[8:9], 8, v64
	v_cmp_gt_i32_e64 s[10:11], 16, v64
	v_cmp_gt_i32_e64 s[12:13], 32, v64
	v_and_b32_e32 v223, 62, v64
	v_lshl_add_u64 v[78:79], v[4:5], 0, v[68:69]
	s_add_i32 s33, s18, 0xa000
	s_mov_b64 s[40:41], 0
	s_mov_b64 s[44:45], 0
	s_add_i32 s66, s53, 0x2000
	s_add_i32 s67, s53, 0x4000
	s_add_i32 s76, s53, 0x6000
	s_movk_i32 s77, 0x100
	s_mov_b64 s[42:43], 0x20000
	s_mov_b32 s78, 0xff800000
	s_brev_b32 s79, 1
	s_mov_b32 s80, 0x2000604
	v_mov_b32_e32 v229, 0xff800000
	v_mov_b32_e32 v230, 0x7f800000
	v_mbcnt_hi_u32_b32 v231, -1, v0
	v_bfrev_b32_e32 v232, 1
	v_bfrev_b32_e32 v233, 0.5
	s_mov_b32 s81, 0
	s_mov_b32 s82, 0
	s_mov_b32 s52, 0
	s_mov_b32 s16, 0
	s_mov_b64 s[48:49], 0
	s_mov_b64 s[34:35], 0
	s_mov_b32 s83, 0

;     template <class Tp> __device__ __forceinline__ Tp* W(size_t off) const { return (Tp*)(ws + off); }
;     template <class Tp> __device__ __forceinline__ const Tp* I(int k) const { return (const Tp*)a->in[k]; }
; template <int QS, int KS, int OS, bool SEL, int QREG, bool MERGE>
; __device__ __forceinline__ void attn_phase(char* lds, const AttnTensors& X, const MergeArgs& MG, int nb, int nh, int nhkv, int sq, int skv, int p0base, int order, int stride, int first, const int wid) {
;     const int W = 1 << 30;
;     const int nqb = sq / QB, nx = (order & ORDER_PAIRED) ? nqb / 2 : nqb;
;     AttnItem it; int k = 0, pass = 0; const int kmax = attn_kmax(stride, order, nb, nh, nhkv, nqb, nx);
;     while (k < kmax && !attn_item_at(k, first, stride, order, nb, nh, nhkv, nqb, nx, it)) ++k;
;     if (k >= kmax) return;
; __global__ void __launch_bounds__(512, 2) fwd_kernel(Args args) {
;     ...
;     if (IN(3)) {
;         att::AttnTensors X{F.W<bf16_t>(WS_QB), F.W<bf16_t>(WS_KB), F.W<bf16_t>(WS_VB), F.W<bf16_t>(WS_YATT), F.W<unsigned>(WS_MASK)};
;         att::MergeArgs MG{F.ws, F.I<float>(IN_CONV_W)};
;         att::attn_phase<DM, 512, DM, true, 6, true>((char*)lds_raw, X, MG, NB, NHEAD, NKVH, SEQ, SEQ, 0, att::ORDER_PAIRED | att::ORDER_XCD, F.G, F.bid, F.wave);
.LBB0_1780:
	s_setprio 0
	s_cmp_lt_i32 s26, 4
	s_cselect_b64 s[0:1], -1, 0
	s_cmp_gt_i32 s27, 3
	s_cselect_b64 s[2:3], -1, 0
	s_and_b64 s[0:1], s[0:1], s[2:3]
	s_andn2_b64 vcc, exec, s[0:1]
	s_cbranch_vccnz .LBB0_2032
	s_abs_i32 s0, s19
	v_cvt_f32_u32_e32 v0, s0
	s_add_i32 s1, s19, 0x1ff
	s_sub_i32 s2, 0xfffffe01, s19
	s_xor_b32 s3, s1, s19
	v_rcp_iflag_f32_e32 v0, v0
	s_max_i32 s1, s1, s2
	s_sub_i32 s2, 0, s0
	s_ashr_i32 s3, s3, 31
	v_mul_f32_e32 v0, 0x4f7ffffe, v0
	v_cvt_u32_f32_e32 v0, v0
	s_mov_b32 s95, 0
	v_readfirstlane_b32 s4, v0
	s_mul_i32 s2, s2, s4
	s_mul_hi_u32 s2, s4, s2
	s_add_i32 s4, s4, s2
	s_mul_hi_u32 s2, s1, s4
	s_mul_i32 s4, s2, s0
	s_sub_i32 s1, s1, s4
	s_add_i32 s5, s2, 1
	s_sub_i32 s4, s1, s0
	s_cmp_ge_u32 s1, s0
	s_cselect_b32 s2, s5, s2
	s_cselect_b32 s1, s4, s1
	s_add_i32 s4, s2, 1
	s_cmp_ge_u32 s1, s0
	s_cselect_b32 s0, s4, s2
	s_xor_b32 s0, s0, s3
	s_sub_i32 s11, s0, s3
	s_cmp_lt_i32 s11, 1
	s_cbranch_scc1 .LBB0_1975
	s_lshl_b32 s7, s18, 2
	s_lshl_b32 s5, s19, 2
	s_mov_b32 s6, 0
	s_mov_b32 s8, s18
	s_branch .LBB0_1784
